# ssd_out<true> (layer 3): same B/C tile staging through LDS as layers 0-2
# speedup vs baseline: 1.0161x; 1.0032x over previous
.LBB0_1268:
	s_and_b32 s19, s27, 7
	s_lshl_b32 s0, s19, 3
	s_add_i32 s20, s0, s22
	s_lshl_b32 s12, s20, 6
	s_ashr_i32 s18, s27, 3
	s_ashr_i32 s13, s12, 31
	s_lshl_b32 s28, s18, 6
	s_lshl_b64 s[14:15], s[12:13], 1
	s_waitcnt vmcnt(8)
	v_or_b32_e32 v30, s28, v171
	v_lshl_add_u64 v[28:29], v[160:161], 0, s[14:15]
	v_mad_i64_i32 v[0:1], s[0:1], v30, s77, v[28:29]
	v_or_b32_e32 v4, 8, v30
	global_load_dwordx4 v[0:3], v[0:1], off
	v_mad_i64_i32 v[4:5], s[0:1], v4, s77, v[28:29]
	v_or_b32_e32 v8, 16, v30
	global_load_dwordx4 v[4:7], v[4:5], off
	v_mad_i64_i32 v[8:9], s[0:1], v8, s77, v[28:29]
	v_or_b32_e32 v12, 24, v30
	global_load_dwordx4 v[8:11], v[8:9], off
	v_mad_i64_i32 v[12:13], s[0:1], v12, s77, v[28:29]
	v_or_b32_e32 v16, 32, v30
	global_load_dwordx4 v[12:15], v[12:13], off
	v_mad_i64_i32 v[16:17], s[0:1], v16, s77, v[28:29]
	v_or_b32_e32 v20, 40, v30
	global_load_dwordx4 v[16:19], v[16:17], off
	v_mad_i64_i32 v[20:21], s[0:1], v20, s77, v[28:29]
	v_or_b32_e32 v24, 48, v30
	global_load_dwordx4 v[20:23], v[20:21], off
	v_mad_i64_i32 v[24:25], s[0:1], v24, s77, v[28:29]
	v_or_b32_e32 v30, 56, v30
	global_load_dwordx4 v[24:27], v[24:25], off
	v_mad_i64_i32 v[28:29], s[0:1], v30, s77, v[28:29]
	global_load_dwordx4 v[28:31], v[28:29], off
	s_lshl_b32 s0, s18, 6
	s_add_i32 s0, s0, s20
	s_lshl_b32 s0, s0, 9
	v_lshl_add_u32 v198, v169, 3, s0
	v_mov_b32_e32 v199, 0
	v_lshl_add_u64 v[198:199], s[24:25], 0, v[198:199]
	s_mov_b64 s[0:1], 0x400000
	s_nop 0
	v_lshl_add_u64 v[198:199], v[198:199], 0, s[0:1]
	global_load_dwordx2 v[198:199], v[198:199], off
	v_lshrrev_b32_e32 v239, 4, v219
	v_and_b32_e32 v240, 15, v219
	v_mul_u32_u24_e32 v241, 0x110, v239
	v_lshl_add_u32 v241, v240, 4, v241
	v_add_u32_e32 v241, 0x16000, v241
	v_add_u32_e32 v239, s28, v239
	v_mul_u32_u24_e32 v239, 0x3000, v239
	v_lshl_add_u32 v239, v240, 4, v239
	v_lshl_add_u32 v239, s19, 8, v239
	v_add_u32_e32 v240, 0x2800, v239
	global_load_dwordx4 v[82:85], v240, s[8:9]
	v_add_u32_e32 v240, 0x62800, v239
	global_load_dwordx4 v[92:95], v240, s[8:9]
	v_add_u32_e32 v240, 0x2000, v239
	global_load_dwordx4 v[96:99], v240, s[8:9]
	v_add_u32_e32 v240, 0x62000, v239
	global_load_dwordx4 v[104:107], v240, s[8:9]
	s_ashr_i32 s21, s20, 31
	v_readlane_b32 s56, v251, 32
	s_lshl_b64 s[16:17], s[20:21], 2
	v_readlane_b32 s58, v251, 34
	v_readlane_b32 s59, v251, 35
	s_add_u32 s0, s58, s16
	s_addc_u32 s1, s59, s17
	v_readlane_b32 s60, v251, 36
	v_readlane_b32 s61, v251, 37
	v_or_b32_e32 v172, s28, v166
	v_lshlrev_b32_e32 v32, 1, v158
	s_movk_i32 s74, 0x2000
	s_movk_i32 s76, 0x1000
	v_readlane_b32 s62, v251, 38
	v_readlane_b32 s63, v251, 39
	v_readlane_b32 s57, v251, 33
	v_readlane_b32 s64, v251, 40
	v_readlane_b32 s65, v251, 41
	v_readlane_b32 s66, v251, 42
	v_readlane_b32 s67, v251, 43
	v_readlane_b32 s68, v251, 44
	v_readlane_b32 s69, v251, 45
	v_readlane_b32 s70, v251, 46
	v_readlane_b32 s71, v251, 47
	s_waitcnt vmcnt(12)
	ds_write_b128 v212, v[0:3]
	s_waitcnt vmcnt(11)
	ds_write_b128 v212, v[4:7] offset:1280
	s_waitcnt vmcnt(10)
	ds_write_b128 v212, v[8:11] offset:2560
	s_waitcnt vmcnt(9)
	ds_write_b128 v212, v[12:15] offset:3840
	s_waitcnt vmcnt(8)
	ds_write_b128 v212, v[16:19] offset:5120
	s_waitcnt vmcnt(7)
	ds_write_b128 v212, v[20:23] offset:6400
	s_waitcnt vmcnt(6)
	ds_write_b128 v212, v[24:27] offset:7680
	s_waitcnt vmcnt(5)
	ds_write_b128 v212, v[28:31] offset:8960
	s_lshl_b32 s86, s19, 8
	s_ashr_i32 s19, s18, 31
	s_waitcnt vmcnt(4)
	ds_write_b32 v183, v198
	ds_write_b32 v184, v199
	s_waitcnt vmcnt(3)
	ds_write_b128 v241, v[82:85]
	s_waitcnt vmcnt(2)
	ds_write_b128 v241, v[92:95] offset:8704
	s_waitcnt vmcnt(1)
	ds_write_b128 v241, v[96:99] offset:17408
	s_waitcnt vmcnt(0)
	ds_write_b128 v241, v[104:107] offset:26112
	v_lshrrev_b32_e32 v238, 4, v219
	v_and_b32_e32 v238, 3, v238
	v_mul_u32_u24_e32 v237, 0x110, v166
	v_lshl_add_u32 v237, v238, 4, v237
	v_add_u32_e32 v237, 0x16000, v237
	v_add_u32_e32 v238, 0x4400, v237
	s_waitcnt lgkmcnt(0)
	s_barrier
	v_mov_b64_e32 v[0:1], s[8:9]
	v_mad_i64_i32 v[0:1], s[0:1], v172, s77, v[0:1]
	v_lshl_add_u64 v[0:1], v[0:1], 0, s[86:87]
	v_lshl_add_u64 v[8:9], v[0:1], 0, v[32:33]
	s_mov_b64 s[0:1], 0x2800
	v_lshl_add_u64 v[74:75], v[8:9], 0, s[0:1]
	v_add_co_u32_e64 v0, s[0:1], s74, v8
	s_movk_i32 s77, 0x3000
	s_nop 0
	v_addc_co_u32_e64 v1, s[0:1], 0, v9, s[0:1]
	s_mov_b32 s0, 0x32000
	s_nop 0
	v_add_co_u32_e64 v30, s[0:1], s0, v8
	ds_read_b128 v[4:7], v237
	s_nop 0
	ds_read_b128 v[0:3], v237 offset:64
	ds_read_b128 v[70:73], v237 offset:128
	ds_read_b128 v[66:69], v237 offset:192
	v_addc_co_u32_e64 v31, s[0:1], 0, v9, s[0:1]
	s_mov_b32 s0, 0x62000
	s_nop 0
	v_add_co_u32_e64 v88, s[0:1], s0, v8
	ds_read_b128 v[62:65], v237 offset:4352
	ds_read_b128 v[58:61], v237 offset:4416
	ds_read_b128 v[54:57], v237 offset:4480
	ds_read_b128 v[50:53], v237 offset:4544
	v_addc_co_u32_e64 v89, s[0:1], 0, v9, s[0:1]
	s_mov_b32 s0, 0x92000
	s_nop 0
	v_add_co_u32_e64 v86, s[0:1], s0, v8
	ds_read_b128 v[46:49], v237 offset:8704
	ds_read_b128 v[42:45], v237 offset:8768
	ds_read_b128 v[38:41], v237 offset:8832
	ds_read_b128 v[24:27], v237 offset:8896
	v_addc_co_u32_e64 v87, s[0:1], 0, v9, s[0:1]
	ds_read_b128 v[20:23], v237 offset:13056
	ds_read_b128 v[16:19], v237 offset:13120
	ds_read_b128 v[8:11], v237 offset:13184
	ds_read_b128 v[12:15], v237 offset:13248
	s_waitcnt lgkmcnt(0)
	ds_read2_b32 v[102:103], v185 offset1:16
	ds_read2_b32 v[28:29], v185 offset0:32 offset1:48
	ds_read_b128 v[82:85], v238
	ds_read_b128 v[92:95], v238 offset:64
	ds_read_b128 v[96:99], v238 offset:128
	ds_read_b128 v[104:107], v238 offset:192
	s_waitcnt lgkmcnt(0)
	v_mfma_f32_16x16x32_bf16 v[74:77], v[82:85], v[4:7], 0
	ds_read_b64 v[100:101], v186
	ds_read_b32 v32, v188
	ds_read_b32 v90, v189
	ds_read_b32 v118, v190
	ds_read_b32 v91, v191
	s_mov_b32 s0, 0x5040100
	v_mfma_f32_16x16x32_bf16 v[74:77], v[92:95], v[0:3], v[74:77]
	v_mfma_f32_16x16x32_bf16 v[74:77], v[96:99], v[70:73], v[74:77]
	v_mfma_f32_16x16x32_bf16 v[108:111], v[82:85], v[62:65], 0
	v_mfma_f32_16x16x32_bf16 v[78:81], v[104:107], v[66:69], v[74:77]
	s_waitcnt lgkmcnt(4)
	s_nop 3
	s_nop 0
	v_sub_f32_e32 v76, v103, v100
	v_min_f32_e32 v76, 0, v76
	v_mfma_f32_16x16x32_bf16 v[108:111], v[92:95], v[58:61], v[108:111]
	v_mul_f32_e32 v76, 0x3fb8aa3b, v76
	v_exp_f32_e32 v114, v76
	v_sub_f32_e32 v76, v103, v101
	v_min_f32_e32 v76, 0, v76
	v_mul_f32_e32 v76, 0x3fb8aa3b, v76
	v_mfma_f32_16x16x32_bf16 v[108:111], v[96:99], v[54:57], v[108:111]
	v_exp_f32_e32 v115, v76
	s_waitcnt lgkmcnt(3)
	v_sub_f32_e32 v76, v103, v32
	s_waitcnt lgkmcnt(1)
	v_sub_f32_e32 v77, v103, v118
	v_min_f32_e32 v76, 0, v76
	v_min_f32_e32 v77, 0, v77
	v_mul_f32_e32 v76, 0x3fb8aa3b, v76
	v_mul_f32_e32 v77, 0x3fb8aa3b, v77
	v_exp_f32_e32 v76, v76
	v_exp_f32_e32 v77, v77
	v_mfma_f32_16x16x32_bf16 v[108:111], v[104:107], v[50:53], v[108:111]
	v_sub_f32_e32 v74, v102, v100
	v_min_f32_e32 v74, 0, v74
	v_mul_f32_e32 v74, 0x3fb8aa3b, v74
	s_waitcnt lgkmcnt(0)
	v_pk_mul_f32 v[76:77], v[90:91], v[76:77]
	v_exp_f32_e32 v119, v74
	v_sub_f32_e32 v74, v102, v101
	s_nop 0
	v_pk_mul_f32 v[76:77], v[76:77], v[110:111]
	v_mfma_f32_16x16x32_bf16 v[110:113], v[82:85], v[46:49], 0
	v_min_f32_e32 v74, 0, v74
	v_mul_f32_e32 v74, 0x3fb8aa3b, v74
	v_exp_f32_e32 v120, v74
	v_mfma_f32_16x16x32_bf16 v[82:85], v[82:85], v[20:23], 0
	v_sub_f32_e32 v74, v102, v32
	v_sub_f32_e32 v75, v102, v118
	v_min_f32_e32 v74, 0, v74
	v_min_f32_e32 v75, 0, v75
	v_mfma_f32_16x16x32_bf16 v[82:85], v[92:95], v[16:19], v[82:85]
	v_mul_f32_e32 v74, 0x3fb8aa3b, v74
	v_mul_f32_e32 v75, 0x3fb8aa3b, v75
	v_exp_f32_e32 v74, v74
	v_exp_f32_e32 v75, v75
	v_mfma_f32_16x16x32_bf16 v[82:85], v[96:99], v[8:11], v[82:85]
	v_mul_f32_e64 v74, v90, v74
	v_mul_f32_e64 v75, v91, v75
	v_mfma_f32_16x16x32_bf16 v[110:113], v[92:95], v[42:45], v[110:113]
	v_mul_f32_e64 v74, v74, v80
	v_mul_f32_e64 v75, v75, v81
	v_sub_f32_e32 v80, v28, v100
	v_min_f32_e32 v80, 0, v80
	v_mfma_f32_16x16x32_bf16 v[92:95], v[104:107], v[12:15], v[82:85]
	v_mul_f32_e32 v80, 0x3fb8aa3b, v80
	v_exp_f32_e32 v116, v80
	v_sub_f32_e32 v80, v28, v101
	v_sub_f32_e32 v82, v29, v100
	v_sub_f32_e32 v83, v29, v101
	v_min_f32_e32 v82, 0, v82
	v_min_f32_e32 v83, 0, v83
	v_mfma_f32_16x16x32_bf16 v[110:113], v[96:99], v[38:41], v[110:113]
	v_mul_f32_e32 v82, 0x3fb8aa3b, v82
	v_mul_f32_e32 v83, 0x3fb8aa3b, v83
	ds_read_b64 v[96:97], v187
	v_min_f32_e32 v80, 0, v80
	v_exp_f32_e32 v82, v82
	v_exp_f32_e32 v83, v83
	v_mul_f32_e32 v80, 0x3fb8aa3b, v80
	v_exp_f32_e32 v117, v80
	v_sub_f32_e32 v80, v28, v32
	v_sub_f32_e32 v32, v29, v32
	v_min_f32_e32 v32, 0, v32
	s_waitcnt lgkmcnt(0)
	v_pk_mul_f32 v[82:83], v[96:97], v[82:83]
	v_mul_f32_e32 v32, 0x3fb8aa3b, v32
	v_sub_f32_e32 v81, v28, v118
	v_pk_mul_f32 v[82:83], v[82:83], v[92:93]
	v_exp_f32_e32 v92, v32
	v_sub_f32_e32 v32, v29, v118
	v_min_f32_e32 v80, 0, v80
	v_min_f32_e32 v81, 0, v81
	v_min_f32_e32 v32, 0, v32
	v_mul_f32_e32 v80, 0x3fb8aa3b, v80
	v_mul_f32_e32 v81, 0x3fb8aa3b, v81
	v_mul_f32_e32 v84, v96, v119
	v_mul_f32_e32 v32, 0x3fb8aa3b, v32
	v_exp_f32_e32 v80, v80
	v_exp_f32_e32 v81, v81
	v_mul_f32_e32 v78, v84, v78
	v_exp_f32_e32 v93, v32
	v_mfma_f32_16x16x32_bf16 v[110:113], v[104:107], v[24:27], v[110:113]
	v_cndmask_b32_e64 v126, v78, 0, s[46:47]
	v_mul_f32_e32 v78, v97, v120
	v_mul_f32_e32 v78, v78, v79
	v_cndmask_b32_e64 v127, 0, v78, s[48:49]
	v_pk_mul_f32 v[78:79], v[96:97], v[114:115]
	v_pk_mul_f32 v[80:81], v[90:91], v[80:81]
	v_pk_mul_f32 v[84:85], v[78:79], v[108:109]
	v_pk_mul_f32 v[78:79], v[96:97], v[116:117]
	v_pk_mul_f32 v[90:91], v[90:91], v[92:93]
	v_pk_mul_f32 v[78:79], v[78:79], v[110:111]
	v_pk_mul_f32 v[90:91], v[90:91], v[94:95]
	ds_read_b128 v[92:95], v238 offset:4352
	ds_read_b128 v[96:99], v238 offset:4416
	ds_read_b128 v[104:107], v238 offset:4480
	ds_read_b128 v[108:111], v238 offset:4544
	s_waitcnt lgkmcnt(0)
	v_pk_mul_f32 v[80:81], v[80:81], v[112:113]
	ds_read_b128 v[112:115], v186 offset:64
	v_mfma_f32_16x16x32_bf16 v[116:119], v[92:95], v[62:65], 0
	s_waitcnt lgkmcnt(0)
	v_sub_f32_e32 v30, v103, v112
	v_min_f32_e32 v30, 0, v30
	v_mul_f32_e32 v30, 0x3fb8aa3b, v30
	v_mfma_f32_16x16x32_bf16 v[120:123], v[92:95], v[46:49], 0
	v_exp_f32_e32 v32, v30
	v_sub_f32_e32 v30, v103, v113
	v_min_f32_e32 v30, 0, v30
	v_mfma_f32_16x16x32_bf16 v[92:95], v[92:95], v[20:23], 0
	v_mul_f32_e32 v30, 0x3fb8aa3b, v30
	v_exp_f32_e32 v128, v30
	v_sub_f32_e32 v100, v28, v112
	v_mfma_f32_16x16x32_bf16 v[116:119], v[96:99], v[58:61], v[116:119]
	v_sub_f32_e32 v101, v28, v113
	v_min_f32_e32 v100, 0, v100
	v_min_f32_e32 v101, 0, v101
	v_mfma_f32_16x16x32_bf16 v[120:123], v[96:99], v[42:45], v[120:123]
	v_mul_f32_e32 v100, 0x3fb8aa3b, v100
	v_mul_f32_e32 v101, 0x3fb8aa3b, v101
	v_exp_f32_e32 v100, v100
	v_mfma_f32_16x16x32_bf16 v[92:95], v[96:99], v[16:19], v[92:95]
	v_sub_f32_e32 v96, v29, v112
	v_min_f32_e32 v96, 0, v96
	v_mul_f32_e32 v96, 0x3fb8aa3b, v96
	v_mfma_f32_16x16x32_bf16 v[116:119], v[104:107], v[54:57], v[116:119]
	v_exp_f32_e32 v101, v101
	v_sub_f32_e32 v30, v103, v114
	v_sub_f32_e32 v31, v103, v115
	v_mfma_f32_16x16x32_bf16 v[120:123], v[104:107], v[38:41], v[120:123]
	v_min_f32_e32 v30, 0, v30
	v_min_f32_e32 v31, 0, v31
	v_sub_f32_e32 v124, v28, v114
	v_mfma_f32_16x16x32_bf16 v[92:95], v[104:107], v[8:11], v[92:95]
	v_exp_f32_e32 v104, v96
	v_sub_f32_e32 v96, v29, v113
	v_min_f32_e32 v96, 0, v96
	v_mul_f32_e32 v96, 0x3fb8aa3b, v96
	v_exp_f32_e32 v105, v96
	ds_read_b128 v[96:99], v187 offset:64
	v_mfma_f32_16x16x32_bf16 v[116:119], v[108:111], v[50:53], v[116:119]
	v_sub_f32_e32 v125, v28, v115
	v_mul_f32_e32 v30, 0x3fb8aa3b, v30
	v_mul_f32_e32 v31, 0x3fb8aa3b, v31
	s_waitcnt lgkmcnt(0)
	v_mul_f32_e32 v32, v96, v32
	v_mfma_f32_16x16x32_bf16 v[120:123], v[108:111], v[24:27], v[120:123]
	s_nop 1
	v_mul_f32_e32 v32, v32, v116
	v_pk_mul_f32 v[100:101], v[96:97], v[100:101]
	v_min_f32_e32 v124, 0, v124
	v_mfma_f32_16x16x32_bf16 v[92:95], v[108:111], v[12:15], v[92:95]
	v_cndmask_b32_e64 v108, v32, 0, s[46:47]
	v_mul_f32_e32 v32, v97, v128
	v_mul_f32_e32 v32, v32, v117
	v_cndmask_b32_e64 v109, 0, v32, s[48:49]
	v_sub_f32_e32 v32, v29, v114
	v_min_f32_e32 v32, 0, v32
	v_pk_mul_f32 v[96:97], v[96:97], v[104:105]
	v_mul_f32_e32 v32, 0x3fb8aa3b, v32
	v_min_f32_e32 v125, 0, v125
	v_pk_mul_f32 v[92:93], v[96:97], v[92:93]
	v_exp_f32_e32 v96, v32
	v_sub_f32_e32 v32, v29, v115
	v_exp_f32_e32 v30, v30
	v_exp_f32_e32 v31, v31
	v_mul_f32_e32 v124, 0x3fb8aa3b, v124
	v_mul_f32_e32 v125, 0x3fb8aa3b, v125
	v_min_f32_e32 v32, 0, v32
	v_exp_f32_e32 v124, v124
	v_exp_f32_e32 v125, v125
	v_mul_f32_e32 v32, 0x3fb8aa3b, v32
	v_exp_f32_e32 v97, v32
	v_pk_mul_f32 v[30:31], v[98:99], v[30:31]
	v_pk_mul_f32 v[100:101], v[100:101], v[120:121]
	v_pk_mul_f32 v[104:105], v[30:31], v[118:119]
	v_pk_mul_f32 v[30:31], v[98:99], v[124:125]
	v_cvt_pk_bf16_f32 v78, v78, v79
	v_pk_mul_f32 v[106:107], v[30:31], v[122:123]
	v_pk_mul_f32 v[30:31], v[98:99], v[96:97]
	v_cvt_pk_bf16_f32 v79, v80, v81
	v_pk_mul_f32 v[94:95], v[30:31], v[94:95]
	v_cvt_pk_bf16_f32 v31, v74, v75
	v_cvt_pk_bf16_f32 v75, v76, v77
	v_cvt_pk_bf16_f32 v77, v104, v105
	v_cvt_pk_bf16_f32 v74, v84, v85
	v_cndmask_b32_e64 v84, v77, 0, s[52:53]
	v_lshrrev_b32_e32 v77, 16, v77
	v_cndmask_b32_e64 v77, v77, 0, s[50:51]
	v_perm_b32 v77, v77, v84, s0
	v_cvt_pk_bf16_f32 v80, v100, v101
	v_cvt_pk_bf16_f32 v81, v106, v107
	v_cvt_pk_bf16_f32 v82, v82, v83
	v_cvt_pk_bf16_f32 v83, v90, v91
	v_cvt_pk_bf16_f32 v84, v92, v93
	v_cvt_pk_bf16_f32 v85, v94, v95
	ds_read_b128 v[90:93], v238 offset:8704
	ds_read_b128 v[94:97], v238 offset:8768
	ds_read_b128 v[98:101], v238 offset:8832
	ds_read_b128 v[104:107], v238 offset:8896
	s_waitcnt lgkmcnt(0)
	v_cvt_pk_bf16_f32 v76, v108, v109
	ds_read_b128 v[108:111], v186 offset:128
	v_mfma_f32_16x16x32_bf16 v[112:115], v[90:93], v[46:49], 0
	s_waitcnt lgkmcnt(0)
	v_sub_f32_e32 v88, v28, v108
	v_min_f32_e32 v88, 0, v88
	v_mul_f32_e32 v88, 0x3fb8aa3b, v88
	v_exp_f32_e32 v118, v88
	v_sub_f32_e32 v88, v28, v109
	v_min_f32_e32 v88, 0, v88
	v_mul_f32_e32 v88, 0x3fb8aa3b, v88
	v_exp_f32_e32 v119, v88
	v_sub_f32_e32 v88, v28, v110
	v_min_f32_e32 v88, 0, v88
	v_mul_f32_e32 v88, 0x3fb8aa3b, v88
	v_exp_f32_e32 v116, v88
	v_sub_f32_e32 v88, v28, v111
	v_min_f32_e32 v88, 0, v88
	v_mul_f32_e32 v88, 0x3fb8aa3b, v88
	v_exp_f32_e32 v117, v88
	v_mfma_f32_16x16x32_bf16 v[88:91], v[90:93], v[20:23], 0
	v_cndmask_b32_e64 v32, v31, 0, s[52:53]
	v_lshrrev_b32_e32 v31, 16, v31
	v_cndmask_b32_e64 v31, v31, 0, s[50:51]
	v_mfma_f32_16x16x32_bf16 v[88:91], v[94:97], v[16:19], v[88:91]
	v_perm_b32 v31, v31, v32, s0
	v_cvt_pk_bf16_f32 v30, v126, v127
	v_mul_f32_e32 v28, 0x3fb8aa3b, v28
	v_mfma_f32_16x16x32_bf16 v[88:91], v[98:101], v[8:11], v[88:91]
	v_exp_f32_e32 v176, v28
	v_mul_f32_e32 v28, 0x3fb8aa3b, v29
	v_exp_f32_e32 v28, v28
	v_mfma_f32_16x16x32_bf16 v[90:93], v[104:107], v[12:15], v[88:91]
	v_mov_b32_e32 v32, v33
	s_nop 1
	s_nop 0
	v_sub_f32_e32 v88, v29, v108
	v_sub_f32_e32 v89, v29, v109
	v_mfma_f32_16x16x32_bf16 v[112:115], v[94:97], v[42:45], v[112:115]
	v_min_f32_e32 v88, 0, v88
	v_min_f32_e32 v89, 0, v89
	v_mul_f32_e32 v88, 0x3fb8aa3b, v88
	v_mul_f32_e32 v89, 0x3fb8aa3b, v89
	ds_read_b128 v[94:97], v187 offset:128
	v_exp_f32_e32 v88, v88
	v_exp_f32_e32 v89, v89
	v_mfma_f32_16x16x32_bf16 v[112:115], v[98:101], v[38:41], v[112:115]
	s_waitcnt lgkmcnt(0)
	v_mul_f32_e32 v98, v94, v118
	v_pk_mul_f32 v[88:89], v[94:95], v[88:89]
	v_mfma_f32_16x16x32_bf16 v[112:115], v[104:107], v[24:27], v[112:115]
	v_mul_f32_e64 v90, v88, v90
	v_mul_f32_e64 v91, v89, v91
	v_sub_f32_e32 v88, v29, v110
	v_min_f32_e32 v88, 0, v88
	v_mul_f32_e32 v88, 0x3fb8aa3b, v88
	v_exp_f32_e32 v94, v88
	v_sub_f32_e32 v88, v29, v111
	v_min_f32_e32 v88, 0, v88
	v_mul_f32_e32 v98, v98, v112
	v_mul_f32_e32 v88, 0x3fb8aa3b, v88
	v_cndmask_b32_e64 v120, v98, 0, s[46:47]
	v_mul_f32_e32 v98, v95, v119
	v_exp_f32_e32 v95, v88
	v_mul_f32_e32 v98, v98, v113
	v_cndmask_b32_e64 v121, 0, v98, s[48:49]
	v_pk_mul_f32 v[88:89], v[96:97], v[116:117]
	v_pk_mul_f32 v[94:95], v[96:97], v[94:95]
	v_pk_mul_f32 v[88:89], v[88:89], v[114:115]
	v_pk_mul_f32 v[92:93], v[94:95], v[92:93]
	ds_read_b128 v[94:97], v238 offset:13056
	ds_read_b128 v[98:101], v238 offset:13120
	ds_read_b128 v[104:107], v238 offset:13184
	ds_read_b128 v[108:111], v238 offset:13248
	s_waitcnt lgkmcnt(0)
	v_mfma_f32_16x16x32_bf16 v[94:97], v[94:97], v[20:23], 0
	ds_read_b128 v[112:115], v186 offset:192
	ds_read_b128 v[116:119], v187 offset:192
	v_cvt_pk_bf16_f32 v90, v90, v91
	v_cvt_pk_bf16_f32 v91, v92, v93
	v_mfma_f32_16x16x32_bf16 v[94:97], v[98:101], v[16:19], v[94:97]
	s_waitcnt lgkmcnt(1)
	v_sub_f32_e32 v86, v29, v112
	v_min_f32_e32 v86, 0, v86
	v_mul_f32_e32 v86, 0x3fb8aa3b, v86
	v_mfma_f32_16x16x32_bf16 v[94:97], v[104:107], v[8:11], v[94:97]
	v_exp_f32_e32 v86, v86
	v_sub_f32_e32 v87, v29, v115
	v_min_f32_e32 v87, 0, v87
	v_mfma_f32_16x16x32_bf16 v[94:97], v[108:111], v[12:15], v[94:97]
	s_waitcnt lgkmcnt(0)
	v_mul_f32_e32 v86, v116, v86
	v_mul_f32_e32 v87, 0x3fb8aa3b, v87
	v_exp_f32_e32 v87, v87
	s_nop 3
	v_mul_f32_e32 v86, v86, v94
	v_cndmask_b32_e64 v98, v86, 0, s[46:47]
	v_sub_f32_e32 v86, v29, v113
	v_min_f32_e32 v86, 0, v86
	v_mul_f32_e32 v86, 0x3fb8aa3b, v86
	v_exp_f32_e32 v86, v86
	s_nop 0
	v_mul_f32_e32 v86, v117, v86
	v_mul_f32_e32 v86, v86, v95
	v_cndmask_b32_e64 v99, 0, v86, s[48:49]
	v_sub_f32_e32 v86, v29, v114
	v_min_f32_e32 v86, 0, v86
	v_mul_f32_e32 v86, 0x3fb8aa3b, v86
	v_exp_f32_e32 v86, v86
	v_cvt_pk_bf16_f32 v92, v98, v99
	v_mul_f32_e32 v98, 0x3fb8aa3b, v102
	v_mul_f32_e32 v102, 0x3fb8aa3b, v103
	v_pk_mul_f32 v[86:87], v[118:119], v[86:87]
	v_exp_f32_e32 v178, v98
	v_pk_mul_f32 v[94:95], v[86:87], v[96:97]
	v_cvt_pk_bf16_f32 v87, v88, v89
	v_cvt_pk_bf16_f32 v93, v94, v95
	v_cndmask_b32_e64 v88, v87, 0, s[52:53]
	v_lshrrev_b32_e32 v87, 16, v87
	v_cndmask_b32_e64 v94, v93, 0, s[52:53]
	v_lshrrev_b32_e32 v93, 16, v93
	v_cndmask_b32_e64 v87, v87, 0, s[50:51]
	v_cndmask_b32_e64 v93, v93, 0, s[50:51]
	v_perm_b32 v87, v87, v88, s0
	v_perm_b32 v93, v93, v94, s0
	s_lshl_b64 s[0:1], s[18:19], 12
	s_lshl_b64 s[18:19], s[20:21], 6
	s_add_u32 s0, s18, s0
	s_addc_u32 s1, s19, s1
	v_mov_b32_e32 v95, s1
	v_or_b32_e32 v94, s0, v166
	v_lshlrev_b64 v[94:95], 8, v[94:95]
	v_lshl_add_u64 v[142:143], v[162:163], 0, v[94:95]
	v_cvt_pk_bf16_f32 v86, v120, v121
	global_load_dwordx4 v[106:109], v[142:143], off
	global_load_dwordx4 v[110:113], v[142:143], off offset:64
	global_load_dwordx4 v[114:117], v[142:143], off offset:128
	global_load_dwordx4 v[118:121], v[142:143], off offset:192
	s_waitcnt vmcnt(3)
	v_mfma_f32_16x16x32_bf16 v[94:97], v[106:109], v[4:7], 0
	v_exp_f32_e32 v174, v102
	v_mov_b32_e32 v88, v33
	v_mfma_f32_16x16x32_bf16 v[98:101], v[106:109], v[62:65], 0
	v_mov_b32_e32 v89, v33
	v_mfma_f32_16x16x32_bf16 v[102:105], v[106:109], v[46:49], 0
	v_mfma_f32_16x16x32_bf16 v[106:109], v[106:109], v[20:23], 0
	s_waitcnt vmcnt(2)
	v_mfma_f32_16x16x32_bf16 v[94:97], v[110:113], v[0:3], v[94:97]
	v_mfma_f32_16x16x32_bf16 v[98:101], v[110:113], v[58:61], v[98:101]
	v_mfma_f32_16x16x32_bf16 v[102:105], v[110:113], v[42:45], v[102:105]
	v_mfma_f32_16x16x32_bf16 v[106:109], v[110:113], v[16:19], v[106:109]
	v_add_co_u32_e64 v110, s[0:1], s76, v142
	s_nop 1
	v_addc_co_u32_e64 v111, s[0:1], 0, v143, s[0:1]
	v_add_co_u32_e64 v126, s[0:1], s74, v142
	s_waitcnt vmcnt(1)
	v_mfma_f32_16x16x32_bf16 v[94:97], v[114:117], v[70:73], v[94:97]
	v_addc_co_u32_e64 v127, s[0:1], 0, v143, s[0:1]
	global_load_dwordx4 v[122:125], v[126:127], off offset:-4096
	global_load_dwordx4 v[128:131], v[110:111], off offset:64
	global_load_dwordx4 v[132:135], v[110:111], off offset:128
	global_load_dwordx4 v[136:139], v[110:111], off offset:192
	v_mfma_f32_16x16x32_bf16 v[98:101], v[114:117], v[54:57], v[98:101]
	v_mfma_f32_16x16x32_bf16 v[102:105], v[114:117], v[38:41], v[102:105]
	v_mfma_f32_16x16x32_bf16 v[106:109], v[114:117], v[8:11], v[106:109]
	s_waitcnt vmcnt(4)
	v_mfma_f32_16x16x32_bf16 v[94:97], v[118:121], v[66:69], v[94:97]
	v_mfma_f32_16x16x32_bf16 v[98:101], v[118:121], v[50:53], v[98:101]
	v_mfma_f32_16x16x32_bf16 v[102:105], v[118:121], v[24:27], v[102:105]
	s_nop 5
	v_mul_f32_e64 v96, v178, v96
	v_mul_f32_e64 v97, v178, v97
	v_pk_mul_f32 v[94:95], v[178:179], v[94:95] op_sel_hi:[0,1]
	v_mfma_f32_16x16x32_bf16 v[106:109], v[118:121], v[12:15], v[106:109]
	s_waitcnt vmcnt(3)
	v_mfma_f32_16x16x32_bf16 v[110:113], v[122:125], v[4:7], 0
	v_mul_f32_e64 v104, v176, v104
	v_mul_f32_e64 v105, v176, v105
	v_pk_mul_f32 v[102:103], v[176:177], v[102:103] op_sel_hi:[0,1]
	s_nop 2
	v_pk_mul_f32 v[108:109], v[28:29], v[108:109] op_sel_hi:[0,1]
	v_mfma_f32_16x16x32_bf16 v[114:117], v[122:125], v[62:65], 0
	v_mul_f32_e64 v106, v28, v106
	v_mul_f32_e64 v107, v28, v107
	v_mfma_f32_16x16x32_bf16 v[118:121], v[122:125], v[46:49], 0
	v_mfma_f32_16x16x32_bf16 v[122:125], v[122:125], v[20:23], 0
	s_waitcnt vmcnt(2)
	v_mfma_f32_16x16x32_bf16 v[110:113], v[128:131], v[0:3], v[110:113]
	v_mfma_f32_16x16x32_bf16 v[114:117], v[128:131], v[58:61], v[114:117]
	v_mfma_f32_16x16x32_bf16 v[118:121], v[128:131], v[42:45], v[118:121]
	v_mfma_f32_16x16x32_bf16 v[122:125], v[128:131], v[16:19], v[122:125]
	s_waitcnt vmcnt(1)
	v_mfma_f32_16x16x32_bf16 v[110:113], v[132:135], v[70:73], v[110:113]
	v_mfma_f32_16x16x32_bf16 v[114:117], v[132:135], v[54:57], v[114:117]
	v_mfma_f32_16x16x32_bf16 v[118:121], v[132:135], v[38:41], v[118:121]
	v_mfma_f32_16x16x32_bf16 v[122:125], v[132:135], v[8:11], v[122:125]
	s_waitcnt vmcnt(0)
	v_mfma_f32_16x16x32_bf16 v[110:113], v[136:139], v[66:69], v[110:113]
	v_mfma_f32_16x16x32_bf16 v[114:117], v[136:139], v[50:53], v[114:117]
	v_mfma_f32_16x16x32_bf16 v[118:121], v[136:139], v[24:27], v[118:121]
	s_nop 5
	v_mul_f32_e64 v112, v178, v112
	v_mul_f32_e64 v113, v178, v113
	v_pk_mul_f32 v[110:111], v[178:179], v[110:111] op_sel_hi:[0,1]
	v_pk_mul_f32 v[116:117], v[174:175], v[116:117] op_sel_hi:[0,1]
	v_mfma_f32_16x16x32_bf16 v[122:125], v[136:139], v[12:15], v[122:125]
	global_load_dwordx4 v[138:141], v[126:127], off
	global_load_dwordx4 v[144:147], v[126:127], off offset:64
	global_load_dwordx4 v[148:151], v[126:127], off offset:128
	global_load_dwordx4 v[152:155], v[126:127], off offset:192
	v_pk_mul_f32 v[114:115], v[174:175], v[114:115] op_sel_hi:[0,1]
	s_waitcnt vmcnt(3)
	v_mfma_f32_16x16x32_bf16 v[126:129], v[138:141], v[4:7], 0
	v_mul_f32_e64 v120, v176, v120
	v_mul_f32_e64 v121, v176, v121
	v_pk_mul_f32 v[118:119], v[176:177], v[118:119] op_sel_hi:[0,1]
	v_pk_mul_f32 v[124:125], v[28:29], v[124:125] op_sel_hi:[0,1]
	v_mfma_f32_16x16x32_bf16 v[130:133], v[138:141], v[62:65], 0
	v_mul_f32_e64 v122, v28, v122
	v_mul_f32_e64 v123, v28, v123
	v_mfma_f32_16x16x32_bf16 v[134:137], v[138:141], v[46:49], 0
	v_mfma_f32_16x16x32_bf16 v[138:141], v[138:141], v[20:23], 0
	s_waitcnt vmcnt(2)
	v_mfma_f32_16x16x32_bf16 v[126:129], v[144:147], v[0:3], v[126:129]
	v_mfma_f32_16x16x32_bf16 v[130:133], v[144:147], v[58:61], v[130:133]
	v_mfma_f32_16x16x32_bf16 v[134:137], v[144:147], v[42:45], v[134:137]
	v_mfma_f32_16x16x32_bf16 v[138:141], v[144:147], v[16:19], v[138:141]
	s_waitcnt vmcnt(1)
	v_mfma_f32_16x16x32_bf16 v[126:129], v[148:151], v[70:73], v[126:129]
	v_mfma_f32_16x16x32_bf16 v[130:133], v[148:151], v[54:57], v[130:133]
	v_mfma_f32_16x16x32_bf16 v[134:137], v[148:151], v[38:41], v[134:137]
	v_mfma_f32_16x16x32_bf16 v[138:141], v[148:151], v[8:11], v[138:141]
	s_waitcnt vmcnt(0)
	v_mfma_f32_16x16x32_bf16 v[126:129], v[152:155], v[66:69], v[126:129]
	v_mfma_f32_16x16x32_bf16 v[130:133], v[152:155], v[50:53], v[130:133]
	v_mfma_f32_16x16x32_bf16 v[134:137], v[152:155], v[24:27], v[134:137]
	s_nop 5
	v_mul_f32_e64 v128, v178, v128
	v_mul_f32_e64 v129, v178, v129
	v_pk_mul_f32 v[126:127], v[178:179], v[126:127] op_sel_hi:[0,1]
	v_pk_mul_f32 v[132:133], v[174:175], v[132:133] op_sel_hi:[0,1]
	v_mfma_f32_16x16x32_bf16 v[138:141], v[152:155], v[12:15], v[138:141]
	v_add_co_u32_e64 v154, s[0:1], s77, v142
	v_pk_mul_f32 v[130:131], v[174:175], v[130:131] op_sel_hi:[0,1]
	s_nop 0
	v_addc_co_u32_e64 v155, s[0:1], 0, v143, s[0:1]
	global_load_dwordx4 v[142:145], v[154:155], off
	global_load_dwordx4 v[146:149], v[154:155], off offset:64
	global_load_dwordx4 v[150:153], v[154:155], off offset:128
	s_nop 0
	global_load_dwordx4 v[154:157], v[154:155], off offset:192
	s_waitcnt vmcnt(3)
	v_mfma_f32_16x16x32_bf16 v[4:7], v[142:145], v[4:7], 0
	v_mul_f32_e64 v136, v176, v136
	v_mul_f32_e64 v137, v176, v137
	v_pk_mul_f32 v[134:135], v[176:177], v[134:135] op_sel_hi:[0,1]
	s_waitcnt vmcnt(2)
	v_mfma_f32_16x16x32_bf16 v[0:3], v[146:149], v[0:3], v[4:7]
	v_mul_f32_e64 v140, v28, v140
	v_mul_f32_e64 v141, v28, v141
	v_pk_mul_f32 v[138:139], v[28:29], v[138:139] op_sel_hi:[0,1]
	s_add_u32 s0, s62, s16
	s_waitcnt vmcnt(1)
	v_mfma_f32_16x16x32_bf16 v[0:3], v[150:153], v[70:73], v[0:3]
	s_addc_u32 s1, s63, s17
	s_waitcnt vmcnt(0)
	v_mfma_f32_16x16x32_bf16 v[0:3], v[154:157], v[66:69], v[0:3]
	s_nop 7
	v_pk_mul_f32 v[68:69], v[178:179], v[2:3] op_sel_hi:[0,1]
	v_pk_mul_f32 v[66:67], v[178:179], v[0:1] op_sel_hi:[0,1]
	v_mfma_f32_16x16x32_bf16 v[0:3], v[142:145], v[62:65], 0
	v_mfma_f32_16x16x32_bf16 v[0:3], v[146:149], v[58:61], v[0:3]
	v_mfma_f32_16x16x32_bf16 v[0:3], v[150:153], v[54:57], v[0:3]
	v_mfma_f32_16x16x32_bf16 v[0:3], v[154:157], v[50:53], v[0:3]
	s_nop 7
	v_pk_mul_f32 v[72:73], v[174:175], v[2:3] op_sel_hi:[0,1]
	v_pk_mul_f32 v[70:71], v[174:175], v[0:1] op_sel_hi:[0,1]
	v_mfma_f32_16x16x32_bf16 v[0:3], v[142:145], v[46:49], 0
	v_mfma_f32_16x16x32_bf16 v[0:3], v[146:149], v[42:45], v[0:3]
	v_mfma_f32_16x16x32_bf16 v[0:3], v[150:153], v[38:41], v[0:3]
	v_mfma_f32_16x16x32_bf16 v[0:3], v[154:157], v[24:27], v[0:3]
	s_nop 7
	v_pk_mul_f32 v[26:27], v[176:177], v[2:3] op_sel_hi:[0,1]
	v_pk_mul_f32 v[24:25], v[176:177], v[0:1] op_sel_hi:[0,1]
	v_mfma_f32_16x16x32_bf16 v[0:3], v[142:145], v[20:23], 0
	v_mfma_f32_16x16x32_bf16 v[0:3], v[146:149], v[16:19], v[0:3]
	v_mul_f32_e64 v18, v174, v100
	v_mul_f32_e64 v19, v174, v101
	v_pk_mul_f32 v[16:17], v[174:175], v[98:99] op_sel_hi:[0,1]
	v_mfma_f32_16x16x32_bf16 v[0:3], v[150:153], v[8:11], v[0:3]
	v_mfma_f32_16x16x32_bf16 v[0:3], v[154:157], v[12:15], v[0:3]
	s_nop 7
	v_pk_mul_f32 v[10:11], v[28:29], v[2:3] op_sel_hi:[0,1]
	v_pk_mul_f32 v[8:9], v[28:29], v[0:1] op_sel_hi:[0,1]
	ds_read_b64_tr_b16 v[2:3], v213 offset:2560
	ds_read_b64_tr_b16 v[0:1], v213
	ds_read_b64_tr_b16 v[4:5], v213 offset:32
	ds_read_b64_tr_b16 v[12:13], v213 offset:5120
	ds_read_b64_tr_b16 v[14:15], v213 offset:7680
	s_waitcnt lgkmcnt(3)
	v_mfma_f32_16x16x32_bf16 v[94:97], v[0:3], v[30:33], v[94:97]
	v_mfma_f32_16x16x32_bf16 v[50:53], v[0:3], v[74:77], v[16:19]
	v_mfma_f32_16x16x32_bf16 v[16:19], v[0:3], v[78:81], v[102:105]
	v_mfma_f32_16x16x32_bf16 v[0:3], v[0:3], v[82:85], v[106:109]
	s_waitcnt lgkmcnt(0)
	v_mfma_f32_16x16x32_bf16 v[38:41], v[12:15], v[86:89], v[16:19]
	v_mfma_f32_16x16x32_bf16 v[12:15], v[12:15], v[90:93], v[0:3]
	ds_read_b64_tr_b16 v[6:7], v213 offset:2592
	s_nop 3
	ds_read_b64_tr_b16 v[0:1], v213 offset:5152
	ds_read_b64_tr_b16 v[2:3], v213 offset:7712
	s_waitcnt lgkmcnt(2)
	v_mfma_f32_16x16x32_bf16 v[62:65], v[4:7], v[30:33], v[110:113]
	v_mfma_f32_16x16x32_bf16 v[46:49], v[4:7], v[74:77], v[114:117]
	v_mfma_f32_16x16x32_bf16 v[16:19], v[4:7], v[78:81], v[118:121]
	v_mfma_f32_16x16x32_bf16 v[4:7], v[4:7], v[82:85], v[122:125]
	s_waitcnt lgkmcnt(0)
	v_mfma_f32_16x16x32_bf16 v[20:23], v[0:3], v[86:89], v[16:19]
	v_mfma_f32_16x16x32_bf16 v[4:7], v[0:3], v[90:93], v[4:7]
	ds_read_b64_tr_b16 v[0:1], v213 offset:64
	ds_read_b64_tr_b16 v[2:3], v213 offset:2624
	ds_read_b64_tr_b16 v[54:55], v213 offset:5184
	ds_read_b64_tr_b16 v[56:57], v213 offset:7744
	ds_read_b64_tr_b16 v[98:99], v213 offset:96
	ds_read_b64_tr_b16 v[100:101], v213 offset:2656
	ds_read_b64_tr_b16 v[102:103], v213 offset:5216
	ds_read_b64_tr_b16 v[104:105], v213 offset:7776
	s_waitcnt lgkmcnt(6)
	v_mfma_f32_16x16x32_bf16 v[58:61], v[0:3], v[30:33], v[126:129]
	v_mfma_f32_16x16x32_bf16 v[42:45], v[0:3], v[74:77], v[130:133]
	v_mfma_f32_16x16x32_bf16 v[16:19], v[0:3], v[78:81], v[134:137]
	v_mfma_f32_16x16x32_bf16 v[0:3], v[0:3], v[82:85], v[138:141]
	s_waitcnt lgkmcnt(4)
	v_mfma_f32_16x16x32_bf16 v[16:19], v[54:57], v[86:89], v[16:19]
	v_mfma_f32_16x16x32_bf16 v[0:3], v[54:57], v[90:93], v[0:3]
	s_waitcnt lgkmcnt(2)
	v_mfma_f32_16x16x32_bf16 v[54:57], v[98:101], v[30:33], v[66:69]
	v_add_u32_e32 v32, v192, v158
	v_mfma_f32_16x16x32_bf16 v[28:31], v[98:101], v[74:77], v[70:73]
	s_nop 0
	ds_read_b64 v[68:69], v32
	v_lshlrev_b32_e32 v32, 1, v170
	global_load_dword v70, v33, s[0:1] offset:768
	s_add_u32 s0, s2, s14
	s_addc_u32 s1, s3, s15
	v_mfma_f32_16x16x32_bf16 v[24:27], v[98:101], v[78:81], v[24:27]
	v_mov_b64_e32 v[78:79], s[0:1]
	v_mad_i64_i32 v[66:67], s[0:1], v172, s96, v[78:79]
	v_lshl_add_u64 v[72:73], v[66:67], 0, v[32:33]
	global_load_dwordx2 v[74:75], v[72:73], off
	global_load_dwordx2 v[202:203], v[72:73], off offset:32
	global_load_dwordx2 v[216:217], v[72:73], off offset:64
	global_load_dwordx2 v[248:249], v[72:73], off offset:96
	s_waitcnt lgkmcnt(0)
	v_lshlrev_b32_e32 v66, 16, v68
	v_and_b32_e32 v67, 0xffff0000, v68
	v_mfma_f32_16x16x32_bf16 v[8:11], v[98:101], v[82:85], v[8:11]
	s_waitcnt vmcnt(4)
	v_pk_fma_f32 v[66:67], v[70:71], v[66:67], v[94:95] op_sel_hi:[0,1,1]
	v_mfma_f32_16x16x32_bf16 v[24:27], v[102:105], v[86:89], v[24:27]
	s_waitcnt vmcnt(3)
	v_lshlrev_b32_e32 v76, 16, v74
	v_mul_f32_e32 v68, 0xbfb8aa3b, v76
	v_exp_f32_e32 v68, v68
	v_and_b32_e32 v77, 0xffff0000, v74
	v_lshlrev_b32_e32 v74, 16, v75
	v_mul_f32_e32 v71, 0xbfb8aa3b, v74
	v_add_f32_e32 v68, 1.0, v68
	v_rcp_f32_e32 v80, v68
	v_mul_f32_e32 v68, 0xbfb8aa3b, v77
	v_exp_f32_e32 v68, v68
	v_exp_f32_e32 v71, v71
	v_pk_mul_f32 v[66:67], v[66:67], v[76:77]
	v_and_b32_e32 v75, 0xffff0000, v75
	v_add_f32_e32 v68, 1.0, v68
	v_rcp_f32_e32 v81, v68
	v_add_f32_e32 v71, 1.0, v71
	v_mfma_f32_16x16x32_bf16 v[8:11], v[102:105], v[90:93], v[8:11]
	v_mul_f32_e64 v66, v66, v80
	v_mul_f32_e64 v67, v67, v81
	v_mul_f32_e32 v68, v67, v67
	v_pk_fma_f32 v[76:77], v[66:67], v[66:67], v[68:69] op_sel_hi:[1,1,0]
	v_lshlrev_b32_e32 v68, 16, v69
	v_and_b32_e32 v69, 0xffff0000, v69
	v_rcp_f32_e32 v80, v71
	v_pk_fma_f32 v[68:69], v[70:71], v[68:69], v[96:97] op_sel_hi:[0,1,1]
	v_mul_f32_e32 v71, 0xbfb8aa3b, v75
	v_exp_f32_e32 v71, v71
	v_pk_mul_f32 v[68:69], v[68:69], v[74:75]
	v_add_f32_e32 v71, 1.0, v71
	v_rcp_f32_e32 v81, v71
	v_add_u32_e32 v71, v192, v193
	v_pk_mul_f32 v[68:69], v[68:69], v[80:81]
	v_pk_fma_f32 v[74:75], v[68:69], v[68:69], v[76:77]
	v_mul_f32_e32 v76, v69, v69
	v_pk_add_f32 v[74:75], v[76:77], v[74:75] op_sel_hi:[0,1]
	ds_read_b64 v[76:77], v71
	s_waitcnt lgkmcnt(0)
	v_lshlrev_b32_e32 v82, 16, v76
	v_and_b32_e32 v83, 0xffff0000, v76
	s_waitcnt vmcnt(2)
	v_mov_b64_e32 v[80:81], v[202:203]
	v_lshlrev_b32_e32 v84, 16, v80
	v_mul_f32_e32 v71, 0xbfb8aa3b, v84
	v_exp_f32_e32 v71, v71
	v_and_b32_e32 v85, 0xffff0000, v80
	v_lshlrev_b32_e32 v80, 16, v81
	v_and_b32_e32 v81, 0xffff0000, v81
	v_add_f32_e32 v71, 1.0, v71
	v_rcp_f32_e32 v86, v71
	v_pk_fma_f32 v[62:63], v[70:71], v[82:83], v[62:63] op_sel_hi:[0,1,1]
	v_mul_f32_e32 v71, 0xbfb8aa3b, v85
	v_exp_f32_e32 v71, v71
	v_pk_mul_f32 v[62:63], v[62:63], v[84:85]
	v_add_f32_e32 v71, 1.0, v71
	v_rcp_f32_e32 v87, v71
	v_mul_f32_e32 v71, 0xbfb8aa3b, v80
	v_exp_f32_e32 v71, v71
	v_pk_mul_f32 v[62:63], v[62:63], v[86:87]
	s_nop 0
	v_pk_fma_f32 v[74:75], v[62:63], v[62:63], v[74:75]
	v_mul_f32_e32 v76, v63, v63
	v_pk_add_f32 v[74:75], v[76:77], v[74:75] op_sel_hi:[0,1]
	v_lshlrev_b32_e32 v76, 16, v77
	v_and_b32_e32 v77, 0xffff0000, v77
	v_add_f32_e32 v71, 1.0, v71
	v_pk_fma_f32 v[64:65], v[70:71], v[76:77], v[64:65] op_sel_hi:[0,1,1]
	v_rcp_f32_e32 v82, v71
	v_pk_mul_f32 v[64:65], v[64:65], v[80:81]
	v_mul_f32_e32 v71, 0xbfb8aa3b, v81
	v_exp_f32_e32 v71, v71
	s_waitcnt vmcnt(1)
	v_mov_b64_e32 v[80:81], v[216:217]
	v_lshlrev_b32_e32 v84, 16, v80
	v_add_f32_e32 v71, 1.0, v71
	v_rcp_f32_e32 v83, v71
	v_add_u32_e32 v71, v192, v194
	v_and_b32_e32 v85, 0xffff0000, v80
	v_lshlrev_b32_e32 v80, 16, v81
	v_pk_mul_f32 v[64:65], v[64:65], v[82:83]
	v_and_b32_e32 v81, 0xffff0000, v81
	v_pk_fma_f32 v[74:75], v[64:65], v[64:65], v[74:75]
	v_mul_f32_e32 v76, v65, v65
	v_pk_add_f32 v[74:75], v[76:77], v[74:75] op_sel_hi:[0,1]
	ds_read_b64 v[76:77], v71
	v_mul_f32_e32 v71, 0xbfb8aa3b, v84
	v_exp_f32_e32 v71, v71
	s_waitcnt lgkmcnt(0)
	v_lshlrev_b32_e32 v82, 16, v76
	v_and_b32_e32 v83, 0xffff0000, v76
	v_add_f32_e32 v71, 1.0, v71
	v_rcp_f32_e32 v86, v71
	v_pk_fma_f32 v[58:59], v[70:71], v[82:83], v[58:59] op_sel_hi:[0,1,1]
	v_mul_f32_e32 v71, 0xbfb8aa3b, v85
	v_exp_f32_e32 v71, v71
	v_pk_mul_f32 v[58:59], v[58:59], v[84:85]
	v_add_f32_e32 v71, 1.0, v71
	v_rcp_f32_e32 v87, v71
	v_mul_f32_e32 v71, 0xbfb8aa3b, v80
	v_exp_f32_e32 v71, v71
	v_pk_mul_f32 v[58:59], v[58:59], v[86:87]
	s_nop 0
	v_pk_fma_f32 v[74:75], v[58:59], v[58:59], v[74:75]
	v_mul_f32_e32 v76, v59, v59
	v_pk_add_f32 v[74:75], v[76:77], v[74:75] op_sel_hi:[0,1]
	v_lshlrev_b32_e32 v76, 16, v77
	v_and_b32_e32 v77, 0xffff0000, v77
	v_add_f32_e32 v71, 1.0, v71
	v_pk_fma_f32 v[60:61], v[70:71], v[76:77], v[60:61] op_sel_hi:[0,1,1]
	v_rcp_f32_e32 v82, v71
	v_pk_mul_f32 v[60:61], v[60:61], v[80:81]
	v_mul_f32_e32 v71, 0xbfb8aa3b, v81
	v_exp_f32_e32 v71, v71
	s_nop 0
	v_add_f32_e32 v71, 1.0, v71
	v_rcp_f32_e32 v83, v71
	v_add_u32_e32 v71, v192, v195
	v_pk_mul_f32 v[60:61], v[60:61], v[82:83]
	s_nop 0
	v_pk_fma_f32 v[74:75], v[60:61], v[60:61], v[74:75]
	v_mul_f32_e32 v76, v61, v61
	v_pk_add_f32 v[74:75], v[76:77], v[74:75] op_sel_hi:[0,1]
	ds_read_b64 v[76:77], v71
	s_waitcnt lgkmcnt(0)
	v_lshlrev_b32_e32 v72, 16, v76
	v_and_b32_e32 v73, 0xffff0000, v76
	s_waitcnt vmcnt(0)
	v_mov_b64_e32 v[80:81], v[248:249]
	v_lshlrev_b32_e32 v82, 16, v80
	v_mul_f32_e32 v71, 0xbfb8aa3b, v82
	v_exp_f32_e32 v71, v71
	v_and_b32_e32 v83, 0xffff0000, v80
	v_lshlrev_b32_e32 v76, 16, v81
	v_add_f32_e32 v71, 1.0, v71
	v_rcp_f32_e32 v84, v71
	v_pk_fma_f32 v[54:55], v[70:71], v[72:73], v[54:55] op_sel_hi:[0,1,1]
	v_mul_f32_e32 v71, 0xbfb8aa3b, v83
	v_exp_f32_e32 v71, v71
	v_pk_mul_f32 v[54:55], v[54:55], v[82:83]
	v_add_f32_e32 v71, 1.0, v71
	v_rcp_f32_e32 v85, v71
	v_mul_f32_e32 v71, 0xbfb8aa3b, v76
	v_exp_f32_e32 v71, v71
	v_pk_mul_f32 v[72:73], v[54:55], v[84:85]
	s_nop 0
	v_pk_fma_f32 v[54:55], v[72:73], v[72:73], v[74:75]
	v_mul_f32_e32 v74, v73, v73
	v_pk_add_f32 v[54:55], v[74:75], v[54:55] op_sel_hi:[0,1]
	v_lshlrev_b32_e32 v74, 16, v77
	v_and_b32_e32 v75, 0xffff0000, v77
	v_and_b32_e32 v77, 0xffff0000, v81
	v_add_f32_e32 v71, 1.0, v71
	v_rcp_f32_e32 v80, v71
	v_pk_fma_f32 v[56:57], v[70:71], v[74:75], v[56:57] op_sel_hi:[0,1,1]
	v_mul_f32_e32 v71, 0xbfb8aa3b, v77
	v_exp_f32_e32 v71, v71
	v_pk_mul_f32 v[56:57], v[56:57], v[76:77]
	v_or_b32_e32 v76, s28, v208
	v_add_f32_e32 v71, 1.0, v71
	v_rcp_f32_e32 v81, v71
	s_nop 0
	v_pk_mul_f32 v[56:57], v[56:57], v[80:81]
	s_nop 0
	v_pk_fma_f32 v[54:55], v[56:57], v[56:57], v[54:55]
	v_mul_f32_e32 v74, v57, v57
	v_pk_add_f32 v[110:111], v[74:75], v[54:55] op_sel_hi:[0,1]
	v_or_b32_e32 v54, s28, v196
	v_mad_i64_i32 v[74:75], s[0:1], v54, s96, v[78:79]
	v_lshl_add_u64 v[74:75], v[74:75], 0, v[32:33]
	global_load_dwordx2 v[126:127], v[74:75], off
	global_load_dwordx2 v[122:123], v[74:75], off offset:32
	global_load_dwordx2 v[116:117], v[74:75], off offset:64
	global_load_dwordx2 v[112:113], v[74:75], off offset:96
	v_mad_i64_i32 v[74:75], s[0:1], v76, s96, v[78:79]
	v_lshl_add_u64 v[74:75], v[74:75], 0, v[32:33]
	global_load_dwordx2 v[106:107], v[74:75], off
	global_load_dwordx2 v[102:103], v[74:75], off offset:32
	global_load_dwordx2 v[98:99], v[74:75], off offset:64
	global_load_dwordx2 v[94:95], v[74:75], off offset:96
	v_or_b32_e32 v74, s28, v210
	v_mad_i64_i32 v[78:79], s[0:1], v74, s96, v[78:79]
	v_lshl_add_u64 v[78:79], v[78:79], 0, v[32:33]
	global_load_dwordx2 v[90:91], v[78:79], off
	global_load_dwordx2 v[86:87], v[78:79], off offset:32
	global_load_dwordx2 v[82:83], v[78:79], off offset:64
	v_add_u32_e32 v55, v197, v158
	global_load_dwordx2 v[78:79], v[78:79], off offset:96
	v_add_u32_e32 v32, v211, v193
	ds_read_b64 v[120:121], v55
	ds_read_b64 v[88:89], v32
	v_add_u32_e32 v55, v197, v193
	v_add_u32_e32 v32, v211, v194
	ds_read_b64 v[124:125], v55
	ds_read_b64 v[84:85], v32
	v_add_u32_e32 v55, v197, v194
	v_add_u32_e32 v32, v211, v195
	ds_read_b64 v[118:119], v55
	ds_read_b64 v[80:81], v32
	v_add_u32_e32 v55, v197, v195
	ds_read_b64 v[114:115], v55
	v_add_u32_e32 v55, v209, v158
	ds_read_b64 v[108:109], v55
	v_add_u32_e32 v55, v209, v193
	ds_read_b64 v[104:105], v55
	v_add_u32_e32 v55, v209, v194
	ds_read_b64 v[100:101], v55
	v_add_u32_e32 v55, v209, v195
	ds_read_b64 v[96:97], v55
	v_add_u32_e32 v55, v211, v158
	ds_read_b64 v[92:93], v55
	s_lshl_b32 s0, s26, 11
	v_mov_b32_e32 v55, v110
	s_add_i32 s14, s0, 0
	s_nop 0
	v_permlane16_swap_b32_e32 v110, v55
	s_add_i32 s14, s14, 0x15000
	v_add_f32_e32 v55, v110, v55
	s_add_i32 s0, s14, s23
	v_mov_b32_e32 v71, v55
	v_lshl_add_u32 v32, v166, 2, s0
	s_nop 0
	v_permlane32_swap_b32_e32 v55, v71
	s_and_saveexec_b64 s[0:1], s[42:43]
	v_add_f32_e32 v55, v55, v71
	ds_write_b32 v32, v55
	s_or_b64 exec, exec, s[0:1]
	s_waitcnt vmcnt(11)
	v_lshlrev_b32_e32 v128, 16, v126
	v_mul_f32_e32 v55, 0xbfb8aa3b, v128
	v_exp_f32_e32 v55, v55
	v_and_b32_e32 v129, 0xffff0000, v126
	v_lshlrev_b32_e32 v126, 16, v127
	v_mov_b32_e32 v71, v70
	v_add_f32_e32 v55, 1.0, v55
	v_rcp_f32_e32 v130, v55
	v_mul_f32_e32 v55, 0xbfb8aa3b, v129
	v_exp_f32_e32 v55, v55
	s_waitcnt lgkmcnt(11)
	v_lshlrev_b32_e32 v110, 16, v120
	v_and_b32_e32 v111, 0xffff0000, v120
	v_pk_fma_f32 v[50:51], v[70:71], v[110:111], v[50:51]
	v_add_f32_e32 v55, 1.0, v55
	v_rcp_f32_e32 v131, v55
	v_mul_f32_e32 v55, 0xbfb8aa3b, v126
	v_exp_f32_e32 v55, v55
	v_and_b32_e32 v127, 0xffff0000, v127
	v_pk_mul_f32 v[50:51], v[50:51], v[128:129]
	v_lshlrev_b32_e32 v120, 16, v121
	v_add_f32_e32 v55, 1.0, v55
	v_rcp_f32_e32 v128, v55
	v_mul_f32_e32 v55, 0xbfb8aa3b, v127
	v_exp_f32_e32 v55, v55
	v_and_b32_e32 v121, 0xffff0000, v121
	v_pk_fma_f32 v[52:53], v[70:71], v[120:121], v[52:53]
	v_pk_mul_f32 v[50:51], v[50:51], v[130:131]
	v_pk_mul_f32 v[52:53], v[52:53], v[126:127]
	v_add_f32_e32 v55, 1.0, v55
	s_waitcnt vmcnt(10)
	v_lshlrev_b32_e32 v126, 16, v122
	v_rcp_f32_e32 v129, v55
	v_mul_f32_e32 v55, 0xbfb8aa3b, v126
	v_exp_f32_e32 v55, v55
	v_and_b32_e32 v127, 0xffff0000, v122
	v_pk_mul_f32 v[52:53], v[52:53], v[128:129]
	v_lshlrev_b32_e32 v122, 16, v123
	v_add_f32_e32 v55, 1.0, v55
	v_rcp_f32_e32 v128, v55
	v_mul_f32_e32 v55, 0xbfb8aa3b, v127
	v_exp_f32_e32 v55, v55
	v_mul_f32_e32 v110, v51, v51
	v_pk_fma_f32 v[110:111], v[50:51], v[50:51], v[110:111] op_sel_hi:[1,1,0]
	v_mul_f32_e32 v120, v53, v53
	v_add_f32_e32 v55, 1.0, v55
	v_rcp_f32_e32 v129, v55
	v_mul_f32_e32 v55, 0xbfb8aa3b, v122
	v_exp_f32_e32 v55, v55
	v_pk_fma_f32 v[110:111], v[52:53], v[52:53], v[110:111]
	v_and_b32_e32 v123, 0xffff0000, v123
	v_pk_add_f32 v[110:111], v[120:121], v[110:111] op_sel_hi:[0,1]
	s_waitcnt lgkmcnt(9)
	v_lshlrev_b32_e32 v120, 16, v124
	v_and_b32_e32 v121, 0xffff0000, v124
	v_pk_fma_f32 v[46:47], v[70:71], v[120:121], v[46:47]
	v_add_f32_e32 v55, 1.0, v55
	v_pk_mul_f32 v[46:47], v[46:47], v[126:127]
	v_rcp_f32_e32 v124, v55
	v_mul_f32_e32 v55, 0xbfb8aa3b, v123
	v_pk_mul_f32 v[46:47], v[46:47], v[128:129]
	v_exp_f32_e32 v55, v55
	v_pk_fma_f32 v[110:111], v[46:47], v[46:47], v[110:111]
	v_mul_f32_e32 v120, v47, v47
	v_pk_add_f32 v[110:111], v[120:121], v[110:111] op_sel_hi:[0,1]
	v_lshlrev_b32_e32 v120, 16, v125
	v_and_b32_e32 v121, 0xffff0000, v125
	v_pk_fma_f32 v[48:49], v[70:71], v[120:121], v[48:49]
	v_add_f32_e32 v55, 1.0, v55
	v_pk_mul_f32 v[48:49], v[48:49], v[122:123]
	s_waitcnt vmcnt(9)
	v_lshlrev_b32_e32 v122, 16, v116
	v_rcp_f32_e32 v125, v55
	v_mul_f32_e32 v55, 0xbfb8aa3b, v122
	v_exp_f32_e32 v55, v55
	v_and_b32_e32 v123, 0xffff0000, v116
	v_pk_mul_f32 v[48:49], v[48:49], v[124:125]
	v_add_f32_e32 v55, 1.0, v55
	v_rcp_f32_e32 v124, v55
	v_mul_f32_e32 v55, 0xbfb8aa3b, v123
	v_exp_f32_e32 v55, v55
	v_pk_fma_f32 v[110:111], v[48:49], v[48:49], v[110:111]
	v_mul_f32_e32 v120, v49, v49
	v_pk_add_f32 v[110:111], v[120:121], v[110:111] op_sel_hi:[0,1]
	v_add_f32_e32 v55, 1.0, v55
	v_rcp_f32_e32 v125, v55
	s_waitcnt lgkmcnt(7)
	v_lshlrev_b32_e32 v120, 16, v118
	v_and_b32_e32 v121, 0xffff0000, v118
	v_pk_fma_f32 v[42:43], v[70:71], v[120:121], v[42:43]
	v_lshlrev_b32_e32 v118, 16, v119
	v_pk_mul_f32 v[42:43], v[42:43], v[122:123]
	v_and_b32_e32 v119, 0xffff0000, v119
	v_pk_mul_f32 v[42:43], v[42:43], v[124:125]
	v_pk_fma_f32 v[44:45], v[70:71], v[118:119], v[44:45]
	v_pk_fma_f32 v[110:111], v[42:43], v[42:43], v[110:111]
	v_mul_f32_e32 v116, v43, v43
	v_pk_add_f32 v[110:111], v[116:117], v[110:111] op_sel_hi:[0,1]
	v_lshlrev_b32_e32 v116, 16, v117
	v_mul_f32_e32 v55, 0xbfb8aa3b, v116
	v_exp_f32_e32 v55, v55
	v_and_b32_e32 v117, 0xffff0000, v117
	s_waitcnt vmcnt(8)
	v_lshlrev_b32_e32 v118, 16, v112
	v_pk_mul_f32 v[44:45], v[44:45], v[116:117]
	v_add_f32_e32 v55, 1.0, v55
	v_rcp_f32_e32 v120, v55
	v_mul_f32_e32 v55, 0xbfb8aa3b, v117
	v_exp_f32_e32 v55, v55
	v_and_b32_e32 v119, 0xffff0000, v112
	v_add_f32_e32 v55, 1.0, v55
	v_rcp_f32_e32 v121, v55
	v_mul_f32_e32 v55, 0xbfb8aa3b, v118
	v_exp_f32_e32 v55, v55
	v_pk_mul_f32 v[44:45], v[44:45], v[120:121]
	s_nop 0
	v_pk_fma_f32 v[110:111], v[44:45], v[44:45], v[110:111]
	v_add_f32_e32 v55, 1.0, v55
	v_rcp_f32_e32 v120, v55
	v_mul_f32_e32 v55, 0xbfb8aa3b, v119
	v_exp_f32_e32 v55, v55
	v_mul_f32_e32 v116, v45, v45
	v_pk_add_f32 v[110:111], v[116:117], v[110:111] op_sel_hi:[0,1]
	s_waitcnt lgkmcnt(5)
	v_lshlrev_b32_e32 v116, 16, v114
	v_add_f32_e32 v55, 1.0, v55
	v_rcp_f32_e32 v121, v55
	v_and_b32_e32 v117, 0xffff0000, v114
	v_pk_fma_f32 v[28:29], v[70:71], v[116:117], v[28:29]
	v_lshlrev_b32_e32 v114, 16, v115
	v_pk_mul_f32 v[28:29], v[28:29], v[118:119]
	v_and_b32_e32 v115, 0xffff0000, v115
	v_pk_mul_f32 v[28:29], v[28:29], v[120:121]
	v_pk_fma_f32 v[30:31], v[70:71], v[114:115], v[30:31]
	v_pk_fma_f32 v[110:111], v[28:29], v[28:29], v[110:111]
	v_mul_f32_e32 v112, v29, v29
	v_pk_add_f32 v[110:111], v[112:113], v[110:111] op_sel_hi:[0,1]
	v_lshlrev_b32_e32 v112, 16, v113
	v_mul_f32_e32 v55, 0xbfb8aa3b, v112
	v_exp_f32_e32 v55, v55
	v_and_b32_e32 v113, 0xffff0000, v113
	v_pk_mul_f32 v[30:31], v[30:31], v[112:113]
	v_add_f32_e32 v55, 1.0, v55
	v_rcp_f32_e32 v116, v55
	v_mul_f32_e32 v55, 0xbfb8aa3b, v113
	v_exp_f32_e32 v55, v55
	s_nop 0
	v_add_f32_e32 v55, 1.0, v55
	v_rcp_f32_e32 v117, v55
	s_nop 0
	v_pk_mul_f32 v[30:31], v[30:31], v[116:117]
	s_nop 0
	v_pk_fma_f32 v[110:111], v[30:31], v[30:31], v[110:111]
	v_mul_f32_e32 v112, v31, v31
	v_pk_add_f32 v[110:111], v[112:113], v[110:111] op_sel_hi:[0,1]
	v_mov_b32_e32 v55, v110
	s_nop 1
	v_permlane16_swap_b32_e32 v110, v55
	v_add_f32_e32 v55, v110, v55
	v_mov_b32_e32 v75, v55
	s_nop 1
	v_permlane32_swap_b32_e32 v55, v75
	s_and_saveexec_b64 s[0:1], s[42:43]
	v_add_f32_e32 v55, v55, v75
	ds_write_b32 v32, v55 offset:64
	s_or_b64 exec, exec, s[0:1]
	s_waitcnt vmcnt(7)
	v_lshlrev_b32_e32 v112, 16, v106
	v_mul_f32_e32 v55, 0xbfb8aa3b, v112
	v_exp_f32_e32 v55, v55
	v_and_b32_e32 v113, 0xffff0000, v106
	s_waitcnt lgkmcnt(4)
	v_lshlrev_b32_e32 v110, 16, v108
	v_and_b32_e32 v111, 0xffff0000, v108
	v_add_f32_e32 v55, 1.0, v55
	v_rcp_f32_e32 v114, v55
	v_mul_f32_e32 v55, 0xbfb8aa3b, v113
	v_exp_f32_e32 v55, v55
	v_pk_fma_f32 v[38:39], v[70:71], v[110:111], v[38:39]
	v_lshlrev_b32_e32 v108, 16, v109
	v_pk_mul_f32 v[38:39], v[38:39], v[112:113]
	v_add_f32_e32 v55, 1.0, v55
	v_rcp_f32_e32 v115, v55
	v_and_b32_e32 v109, 0xffff0000, v109
	v_pk_fma_f32 v[40:41], v[70:71], v[108:109], v[40:41]
	v_pk_mul_f32 v[38:39], v[38:39], v[114:115]
	s_nop 0
	v_mul_f32_e32 v106, v39, v39
	v_pk_fma_f32 v[110:111], v[38:39], v[38:39], v[106:107] op_sel_hi:[1,1,0]
	v_lshlrev_b32_e32 v106, 16, v107
	v_mul_f32_e32 v55, 0xbfb8aa3b, v106
	v_exp_f32_e32 v55, v55
	v_and_b32_e32 v107, 0xffff0000, v107
	v_pk_mul_f32 v[40:41], v[40:41], v[106:107]
	v_add_f32_e32 v55, 1.0, v55
	v_rcp_f32_e32 v112, v55
	v_mul_f32_e32 v55, 0xbfb8aa3b, v107
	v_exp_f32_e32 v55, v55
	s_nop 0
	v_add_f32_e32 v55, 1.0, v55
	v_rcp_f32_e32 v113, v55
	s_nop 0
	v_pk_mul_f32 v[40:41], v[40:41], v[112:113]
	s_nop 0
	v_pk_fma_f32 v[106:107], v[40:41], v[40:41], v[110:111]
	s_waitcnt vmcnt(6)
	v_lshlrev_b32_e32 v110, 16, v102
	v_mul_f32_e32 v55, 0xbfb8aa3b, v110
	v_exp_f32_e32 v55, v55
	v_and_b32_e32 v111, 0xffff0000, v102
	v_mul_f32_e32 v108, v41, v41
	v_pk_add_f32 v[106:107], v[108:109], v[106:107] op_sel_hi:[0,1]
	v_add_f32_e32 v55, 1.0, v55
	v_rcp_f32_e32 v112, v55
	v_mul_f32_e32 v55, 0xbfb8aa3b, v111
	v_exp_f32_e32 v55, v55
	s_waitcnt lgkmcnt(3)
	v_lshlrev_b32_e32 v108, 16, v104
	v_and_b32_e32 v109, 0xffff0000, v104
	v_pk_fma_f32 v[20:21], v[70:71], v[108:109], v[20:21]
	v_add_f32_e32 v55, 1.0, v55
	v_rcp_f32_e32 v113, v55
	v_pk_mul_f32 v[20:21], v[20:21], v[110:111]
	v_lshlrev_b32_e32 v104, 16, v105
	v_and_b32_e32 v105, 0xffff0000, v105
	v_pk_mul_f32 v[20:21], v[20:21], v[112:113]
	v_pk_fma_f32 v[22:23], v[70:71], v[104:105], v[22:23]
	v_pk_fma_f32 v[106:107], v[20:21], v[20:21], v[106:107]
	v_mul_f32_e32 v102, v21, v21
	v_pk_add_f32 v[106:107], v[102:103], v[106:107] op_sel_hi:[0,1]
	v_lshlrev_b32_e32 v102, 16, v103
	v_mul_f32_e32 v55, 0xbfb8aa3b, v102
	v_exp_f32_e32 v55, v55
	v_and_b32_e32 v103, 0xffff0000, v103
	v_pk_mul_f32 v[22:23], v[22:23], v[102:103]
	v_add_f32_e32 v55, 1.0, v55
	v_rcp_f32_e32 v108, v55
	v_mul_f32_e32 v55, 0xbfb8aa3b, v103
	v_exp_f32_e32 v55, v55
	s_nop 0
	v_add_f32_e32 v55, 1.0, v55
	v_rcp_f32_e32 v109, v55
	s_nop 0
	v_pk_mul_f32 v[22:23], v[22:23], v[108:109]
	s_nop 0
	v_pk_fma_f32 v[102:103], v[22:23], v[22:23], v[106:107]
	s_waitcnt vmcnt(5)
	v_lshlrev_b32_e32 v106, 16, v98
	v_mul_f32_e32 v55, 0xbfb8aa3b, v106
	v_exp_f32_e32 v55, v55
	v_and_b32_e32 v107, 0xffff0000, v98
	v_mul_f32_e32 v104, v23, v23
	v_pk_add_f32 v[102:103], v[104:105], v[102:103] op_sel_hi:[0,1]
	v_add_f32_e32 v55, 1.0, v55
	v_rcp_f32_e32 v108, v55
	v_mul_f32_e32 v55, 0xbfb8aa3b, v107
	v_exp_f32_e32 v55, v55
	s_waitcnt lgkmcnt(2)
	v_lshlrev_b32_e32 v104, 16, v100
	v_and_b32_e32 v105, 0xffff0000, v100
	v_pk_fma_f32 v[16:17], v[70:71], v[104:105], v[16:17]
	v_add_f32_e32 v55, 1.0, v55
	v_rcp_f32_e32 v109, v55
	v_pk_mul_f32 v[16:17], v[16:17], v[106:107]
	v_lshlrev_b32_e32 v100, 16, v101
	v_and_b32_e32 v101, 0xffff0000, v101
	v_pk_mul_f32 v[16:17], v[16:17], v[108:109]
	v_pk_fma_f32 v[18:19], v[70:71], v[100:101], v[18:19]
	v_pk_fma_f32 v[102:103], v[16:17], v[16:17], v[102:103]
	v_mul_f32_e32 v98, v17, v17
	v_pk_add_f32 v[102:103], v[98:99], v[102:103] op_sel_hi:[0,1]
	v_lshlrev_b32_e32 v98, 16, v99
	v_mul_f32_e32 v55, 0xbfb8aa3b, v98
	v_exp_f32_e32 v55, v55
	v_and_b32_e32 v99, 0xffff0000, v99
	v_pk_mul_f32 v[18:19], v[18:19], v[98:99]
	v_add_f32_e32 v55, 1.0, v55
	v_rcp_f32_e32 v104, v55
	v_mul_f32_e32 v55, 0xbfb8aa3b, v99
	v_exp_f32_e32 v55, v55
	s_nop 0
	v_add_f32_e32 v55, 1.0, v55
	v_rcp_f32_e32 v105, v55
	s_nop 0
	v_pk_mul_f32 v[18:19], v[18:19], v[104:105]
	s_nop 0
	v_pk_fma_f32 v[98:99], v[18:19], v[18:19], v[102:103]
	s_waitcnt vmcnt(4)
	v_lshlrev_b32_e32 v102, 16, v94
	v_mul_f32_e32 v55, 0xbfb8aa3b, v102
	v_exp_f32_e32 v55, v55
	v_and_b32_e32 v103, 0xffff0000, v94
	v_mul_f32_e32 v100, v19, v19
	v_pk_add_f32 v[98:99], v[100:101], v[98:99] op_sel_hi:[0,1]
	v_add_f32_e32 v55, 1.0, v55
	v_rcp_f32_e32 v104, v55
	v_mul_f32_e32 v55, 0xbfb8aa3b, v103
	v_exp_f32_e32 v55, v55
	s_waitcnt lgkmcnt(1)
	v_lshlrev_b32_e32 v100, 16, v96
	v_and_b32_e32 v101, 0xffff0000, v96
	v_pk_fma_f32 v[24:25], v[70:71], v[100:101], v[24:25]
	v_add_f32_e32 v55, 1.0, v55
	v_rcp_f32_e32 v105, v55
	v_pk_mul_f32 v[24:25], v[24:25], v[102:103]
	v_lshlrev_b32_e32 v96, 16, v97
	v_and_b32_e32 v97, 0xffff0000, v97
	v_pk_mul_f32 v[24:25], v[24:25], v[104:105]
	v_pk_fma_f32 v[26:27], v[70:71], v[96:97], v[26:27]
	v_pk_fma_f32 v[98:99], v[24:25], v[24:25], v[98:99]
	v_mul_f32_e32 v94, v25, v25
	v_pk_add_f32 v[98:99], v[94:95], v[98:99] op_sel_hi:[0,1]
	v_lshlrev_b32_e32 v94, 16, v95
	v_mul_f32_e32 v55, 0xbfb8aa3b, v94
	v_exp_f32_e32 v55, v55
	v_and_b32_e32 v95, 0xffff0000, v95
	v_pk_mul_f32 v[26:27], v[26:27], v[94:95]
	v_add_f32_e32 v55, 1.0, v55
	v_rcp_f32_e32 v100, v55
	v_mul_f32_e32 v55, 0xbfb8aa3b, v95
	v_exp_f32_e32 v55, v55
	s_nop 0
	v_add_f32_e32 v55, 1.0, v55
	v_rcp_f32_e32 v101, v55
	s_nop 0
	v_pk_mul_f32 v[26:27], v[26:27], v[100:101]
	s_nop 0
	v_pk_fma_f32 v[94:95], v[26:27], v[26:27], v[98:99]
	v_mul_f32_e32 v96, v27, v27
	v_pk_add_f32 v[94:95], v[96:97], v[94:95] op_sel_hi:[0,1]
	v_mov_b32_e32 v55, v94
	s_nop 1
	v_permlane16_swap_b32_e32 v94, v55
	v_add_f32_e32 v55, v94, v55
	v_mov_b32_e32 v75, v55
	s_nop 1
	v_permlane32_swap_b32_e32 v55, v75
	s_and_saveexec_b64 s[0:1], s[42:43]
	v_readlane_b32 s72, v254, 1
	v_readlane_b32 s70, v254, 2
	v_readlane_b32 s71, v254, 3
	v_readlane_b32 s73, v254, 4
	s_mov_b32 s75, 0x8000
	s_mov_b32 s78, 0x200000
	s_mov_b32 s79, 0x7ffff
	v_add_f32_e32 v55, v55, v75
	ds_write_b32 v32, v55 offset:128
	s_or_b64 exec, exec, s[0:1]
	s_waitcnt vmcnt(3)
	v_lshlrev_b32_e32 v96, 16, v90
	v_mul_f32_e32 v55, 0xbfb8aa3b, v96
	v_exp_f32_e32 v55, v55
	v_and_b32_e32 v97, 0xffff0000, v90
	v_lshlrev_b32_e32 v90, 16, v91
	s_waitcnt lgkmcnt(0)
	v_lshlrev_b32_e32 v94, 16, v92
	v_add_f32_e32 v55, 1.0, v55
	v_rcp_f32_e32 v98, v55
	v_mul_f32_e32 v55, 0xbfb8aa3b, v97
	v_exp_f32_e32 v55, v55
	v_and_b32_e32 v95, 0xffff0000, v92
	v_pk_fma_f32 v[12:13], v[70:71], v[94:95], v[12:13]
	v_and_b32_e32 v91, 0xffff0000, v91
	v_add_f32_e32 v55, 1.0, v55
	v_rcp_f32_e32 v99, v55
	v_mul_f32_e32 v55, 0xbfb8aa3b, v90
	v_exp_f32_e32 v55, v55
	v_pk_mul_f32 v[12:13], v[12:13], v[96:97]
	v_lshlrev_b32_e32 v92, 16, v93
	v_and_b32_e32 v93, 0xffff0000, v93
	v_add_f32_e32 v55, 1.0, v55
	v_rcp_f32_e32 v96, v55
	v_mul_f32_e32 v55, 0xbfb8aa3b, v91
	v_exp_f32_e32 v55, v55
	v_pk_mul_f32 v[94:95], v[12:13], v[98:99]
	v_pk_fma_f32 v[14:15], v[70:71], v[92:93], v[14:15]
	v_mul_f32_e32 v12, v95, v95
	v_add_f32_e32 v55, 1.0, v55
	v_rcp_f32_e32 v97, v55
	v_pk_mul_f32 v[14:15], v[14:15], v[90:91]
	v_pk_fma_f32 v[12:13], v[94:95], v[94:95], v[12:13] op_sel_hi:[1,1,0]
	s_waitcnt vmcnt(2)
	v_lshlrev_b32_e32 v92, 16, v86
	v_pk_mul_f32 v[90:91], v[14:15], v[96:97]
	v_and_b32_e32 v93, 0xffff0000, v86
	v_pk_fma_f32 v[12:13], v[90:91], v[90:91], v[12:13]
	v_mul_f32_e32 v14, v91, v91
	v_pk_add_f32 v[12:13], v[14:15], v[12:13] op_sel_hi:[0,1]
	v_lshlrev_b32_e32 v14, 16, v88
	v_and_b32_e32 v15, 0xffff0000, v88
	v_mul_f32_e32 v55, 0xbfb8aa3b, v92
	v_pk_fma_f32 v[4:5], v[70:71], v[14:15], v[4:5]
	v_mul_f32_e32 v14, 0xbfb8aa3b, v93
	v_exp_f32_e32 v55, v55
	v_exp_f32_e32 v14, v14
	v_pk_mul_f32 v[4:5], v[4:5], v[92:93]
	v_and_b32_e32 v15, 0xffff0000, v87
	v_add_f32_e32 v55, 1.0, v55
	v_add_f32_e32 v14, 1.0, v14
	v_rcp_f32_e32 v96, v55
	v_rcp_f32_e32 v97, v14
	v_lshlrev_b32_e32 v14, 16, v87
	v_mul_f32_e32 v55, 0xbfb8aa3b, v14
	v_exp_f32_e32 v55, v55
	v_pk_mul_f32 v[92:93], v[4:5], v[96:97]
	v_add_f32_e32 v55, 1.0, v55
	v_pk_fma_f32 v[4:5], v[92:93], v[92:93], v[12:13]
	v_mul_f32_e32 v12, v93, v93
	v_pk_add_f32 v[4:5], v[12:13], v[4:5] op_sel_hi:[0,1]
	v_lshlrev_b32_e32 v12, 16, v89
	v_and_b32_e32 v13, 0xffff0000, v89
	v_pk_fma_f32 v[6:7], v[70:71], v[12:13], v[6:7]
	v_mul_f32_e32 v12, 0xbfb8aa3b, v15
	v_exp_f32_e32 v12, v12
	v_rcp_f32_e32 v86, v55
	v_pk_mul_f32 v[6:7], v[6:7], v[14:15]
	s_waitcnt vmcnt(1)
	v_and_b32_e32 v13, 0xffff0000, v82
	v_add_f32_e32 v12, 1.0, v12
	v_rcp_f32_e32 v87, v12
	v_lshlrev_b32_e32 v12, 16, v82
	v_mul_f32_e32 v14, 0xbfb8aa3b, v12
	v_exp_f32_e32 v14, v14
	v_pk_mul_f32 v[86:87], v[6:7], v[86:87]
	v_add_f32_e32 v14, 1.0, v14
	v_pk_fma_f32 v[4:5], v[86:87], v[86:87], v[4:5]
	v_mul_f32_e32 v6, v87, v87
	v_pk_add_f32 v[4:5], v[6:7], v[4:5] op_sel_hi:[0,1]
	v_lshlrev_b32_e32 v6, 16, v84
	v_and_b32_e32 v7, 0xffff0000, v84
	v_pk_fma_f32 v[0:1], v[70:71], v[6:7], v[0:1]
	v_mul_f32_e32 v6, 0xbfb8aa3b, v13
	v_exp_f32_e32 v6, v6
	v_rcp_f32_e32 v14, v14
	v_pk_mul_f32 v[0:1], v[0:1], v[12:13]
	v_and_b32_e32 v7, 0xffff0000, v83
	v_add_f32_e32 v6, 1.0, v6
	v_rcp_f32_e32 v15, v6
	v_lshlrev_b32_e32 v6, 16, v83
	v_mul_f32_e32 v12, 0xbfb8aa3b, v6
	v_exp_f32_e32 v12, v12
	v_pk_mul_f32 v[88:89], v[0:1], v[14:15]
	v_add_f32_e32 v12, 1.0, v12
	v_pk_fma_f32 v[0:1], v[88:89], v[88:89], v[4:5]
	v_mul_f32_e32 v4, v89, v89
	v_pk_add_f32 v[0:1], v[4:5], v[0:1] op_sel_hi:[0,1]
	v_lshlrev_b32_e32 v4, 16, v85
	v_and_b32_e32 v5, 0xffff0000, v85
	v_pk_fma_f32 v[2:3], v[70:71], v[4:5], v[2:3]
	v_mul_f32_e32 v4, 0xbfb8aa3b, v7
	v_exp_f32_e32 v4, v4
	v_rcp_f32_e32 v12, v12
	v_pk_mul_f32 v[2:3], v[2:3], v[6:7]
	s_waitcnt vmcnt(0)
	v_and_b32_e32 v5, 0xffff0000, v78
	v_add_f32_e32 v4, 1.0, v4
	v_rcp_f32_e32 v13, v4
	v_lshlrev_b32_e32 v4, 16, v78
	v_mul_f32_e32 v6, 0xbfb8aa3b, v4
	v_exp_f32_e32 v6, v6
	v_pk_mul_f32 v[82:83], v[2:3], v[12:13]
	v_add_f32_e32 v6, 1.0, v6
	v_pk_fma_f32 v[0:1], v[82:83], v[82:83], v[0:1]
	v_mul_f32_e32 v2, v83, v83
	v_pk_add_f32 v[0:1], v[2:3], v[0:1] op_sel_hi:[0,1]
	v_lshlrev_b32_e32 v2, 16, v80
	v_and_b32_e32 v3, 0xffff0000, v80
	v_pk_fma_f32 v[2:3], v[70:71], v[2:3], v[8:9]
	v_rcp_f32_e32 v6, v6
	v_pk_mul_f32 v[2:3], v[2:3], v[4:5]
	v_mul_f32_e32 v4, 0xbfb8aa3b, v5
	v_exp_f32_e32 v4, v4
	v_and_b32_e32 v5, 0xffff0000, v79
	v_add_f32_e32 v4, 1.0, v4
	v_rcp_f32_e32 v7, v4
	v_lshlrev_b32_e32 v4, 16, v79
	v_pk_mul_f32 v[84:85], v[2:3], v[6:7]
	s_nop 0
	v_pk_fma_f32 v[0:1], v[84:85], v[84:85], v[0:1]
	v_mul_f32_e32 v2, v85, v85
	v_pk_add_f32 v[0:1], v[2:3], v[0:1] op_sel_hi:[0,1]
	v_lshlrev_b32_e32 v2, 16, v81
	v_and_b32_e32 v3, 0xffff0000, v81
	v_pk_fma_f32 v[2:3], v[70:71], v[2:3], v[10:11]
	v_mul_f32_e32 v6, 0xbfb8aa3b, v4
	v_pk_mul_f32 v[2:3], v[2:3], v[4:5]
	v_mul_f32_e32 v4, 0xbfb8aa3b, v5
	v_exp_f32_e32 v6, v6
	v_exp_f32_e32 v4, v4
	v_add_f32_e32 v6, 1.0, v6
	v_add_f32_e32 v4, 1.0, v4
	v_rcp_f32_e32 v6, v6
	v_rcp_f32_e32 v7, v4
	s_nop 0
	v_pk_mul_f32 v[70:71], v[2:3], v[6:7]
	s_nop 0
	v_pk_fma_f32 v[0:1], v[70:71], v[70:71], v[0:1]
	v_mul_f32_e32 v2, v71, v71
	v_pk_add_f32 v[0:1], v[2:3], v[0:1] op_sel_hi:[0,1]
	v_mov_b32_e32 v1, v0
	s_nop 1
	v_permlane16_swap_b32_e32 v0, v1
	v_add_f32_e32 v0, v0, v1
	v_mov_b32_e32 v1, v0
	s_nop 1
	v_permlane32_swap_b32_e32 v0, v1
	s_and_saveexec_b64 s[0:1], s[42:43]
	s_cbranch_execz .LBB0_1267
	v_add_f32_e32 v0, v0, v1
	ds_write_b32 v32, v0 offset:192
	s_branch .LBB0_1267
